# diff attention unit prologue: all Q / key-norm / first K,V tile loads issued together (one memory round trip instead of seven) + dead v_mov removal
# baseline (speedup 1.0000x reference)
; #define LAS __attribute__((address_space(3)))
;     ...
;         const int qi = 16 - u / 32, bh = u % 32, b = bh >> 2, h = bh & 3;
;         const int q0 = qi == 0 ? 0 : 16 + 256 * (qi - 1), nkt = qi == 0 ? 1 : 4 * qi + 1;
;         const int q0w = q0 + 32 * wave, qpos = q0w + l31;
;         const bool wave_on = (qi > 0) || (wave == 0);
;         const size_t qrow = (size_t)b * LT + (qpos < LT ? qpos : LT - 1);
;         LAS bf16x8* Qs = (LAS bf16x8*)(lds + 4096 + 4 * DF_KB) + wave * 384 + lane;
;         const float farb = btab[h * 132 + 128] * c2;
;         float mref[2];
;         { const unsigned* kmx = (const unsigned*)(ws + WS_CTL) + CW_KMX + l * 256 + b * 8 + h * 2;
; #pragma unroll
;           for (int c = 0; c < 2; ++c) { float qn2 = 0.f;
; #pragma unroll
;               for (int s = 0; s < 2; ++s) { const u32x4 qv = *(const u32x4*)(U + qrow * INW + C_QD + h * 64 + c * 32 + s * 16 + hi * 8);
;                   const unsigned qw[4] = {qv.x, qv.y, qv.z, qv.w};
;                   { u32x4 qs; qs.x = pkbf(bflo(qw[0]) * c2, bfhi(qw[0]) * c2); qs.y = pkbf(bflo(qw[1]) * c2, bfhi(qw[1]) * c2); qs.z = pkbf(bflo(qw[2]) * c2, bfhi(qw[2]) * c2); qs.w = pkbf(bflo(qw[3]) * c2, bfhi(qw[3]) * c2);
;                     Qs[(c * 2 + s) * 64] = __builtin_bit_cast(bf16x8, qs); }
; #pragma unroll
;                   for (int e = 0; e < 4; ++e) qn2 += bflo(qw[e]) * bflo(qw[e]) + bfhi(qw[e]) * bfhi(qw[e]); }
;               qn2 += __shfl_xor(qn2, 32);
;               const float km2 = __uint_as_float(__hip_atomic_load(kmx + c, __ATOMIC_RELAXED, __HIP_MEMORY_SCOPE_AGENT));
;               mref[c] = (sqrtf(qn2 * km2) * 1.001f + btab[h * 132 + 129]) * c2;
;               { u32x4 qx; qx.x = hi ? 0u : (pkbf(farb - mref[c], 0.f) & 0xffffu); qx.y = 0u; qx.z = 0u; qx.w = 0u; Qs[(4 + c) * 64] = __builtin_bit_cast(bf16x8, qx); } } }
;     ...
;         const bf16_t* kbase = U + (size_t)b * LT * INW + C_KD + h * 64;
;         const bf16_t* vbase = VT + (size_t)bh * 64 * LTP;
;         const unsigned koff = (unsigned)(krow * INW + kch * 8), voff = (unsigned)(krow * LTP + kch * 8);
;         const float farraw = btab[h * 132 + 128];
;         u32x4 kreg = *(const u32x4*)(kbase + koff), vreg = *(const u32x4*)(vbase + voff);
;         *(LAS u32x4*)(KV + krow * DF_PITCH + kch * 16) = kreg; *(LAS u32x4*)(KV + 2 * DF_KB + krow * DF_PITCH + kch * 16) = vreg;
.LBB0_774:
	s_or_b64 exec, exec, s[0:1]
	s_waitcnt lgkmcnt(0)
	s_barrier
	ds_read_b32 v0, v1 offset:2112
	s_movk_i32 s0, 0x21f
	s_waitcnt lgkmcnt(0)
	v_cmp_lt_i32_e32 vcc, s0, v0
	v_readfirstlane_b32 s30, v0
	s_mov_b64 s[0:1], -1
	s_cbranch_vccnz .LBB0_769
	s_ashr_i32 s0, s30, 31
	s_lshr_b32 s0, s0, 27
	s_add_i32 s0, s30, s0
	s_ashr_i32 s35, s0, 5
	s_andn2_b32 s0, s0, 31
	s_sub_i32 s34, s30, s0
	s_lshl_b32 s1, s35, 8
	s_sub_i32 s31, 16, s35
	s_ashr_i32 s0, s34, 2
	s_and_b32 s36, s34, 3
	s_sub_i32 s1, 0xf10, s1
	s_cmp_lg_u32 s31, 0
	s_cselect_b32 s49, s1, 0
	s_add_i32 s49, s49, s46
	s_mul_i32 s22, s0, 0x1010
	s_mul_i32 s1, s36, 0x210
	s_lshl_b32 s0, s0, 3
	v_add_u32_e32 v148, s49, v149
	s_add_i32 s50, s1, 0
	s_ashr_i32 s1, s0, 31
	s_ashr_i32 s23, s22, 31
	v_min_i32_e32 v2, 0x100f, v148
	s_lshl_b64 s[0:1], s[0:1], 2
	v_ashrrev_i32_e32 v3, 31, v2
	s_add_u32 s0, s47, s0
	v_lshl_add_u64 v[2:3], v[2:3], 0, s[22:23]
	s_addc_u32 s1, s48, s1
	s_lshl_b32 s28, s36, 3
	v_mov_b64_e32 v[4:5], s[8:9]
	s_add_u32 s24, s0, s28
	v_mad_u64_u32 v[4:5], s[38:39], v2, s97, v[4:5]
	s_addc_u32 s25, s1, 0
	v_mad_i32_i24 v5, v3, s97, v5
	s_lshl_b32 s40, s36, 7
	v_lshl_add_u64 v[2:3], v[4:5], 0, s[40:41]
	v_mov_b32_e32 v147, v1
	v_lshl_add_u64 v[4:5], v[2:3], 0, v[146:147]
	global_load_dwordx4 v[6:9], v[4:5], off offset:1024
	global_load_dwordx4 v[112:115], v[4:5], off offset:1056
	v_mov_b32_e32 v125, s28
	s_mul_i32 s58, s22, 0x1600
	global_load_dword v124, v125, s[0:1] sc1
	s_mul_hi_i32 s59, s22, 0x1600
	global_load_dwordx4 v[116:119], v[4:5], off offset:1088
	s_add_u32 s58, s8, s58
	s_addc_u32 s59, s9, s59
	global_load_dwordx4 v[120:123], v[4:5], off offset:1120
	s_lshl_b32 s60, s36, 7
	s_add_u32 s58, s58, s60
	s_addc_u32 s59, s59, 0
	global_load_dword v126, v1, s[24:25] offset:4 sc1
	s_mul_i32 s60, s34, 0x41000
	s_ashr_i32 s61, s60, 31
	s_lshl_b64 s[60:61], s[60:61], 1
	s_add_u32 s60, s42, s60
	s_addc_u32 s61, s43, s61
	v_lshl_add_u64 v[66:67], v[142:143], 1, s[58:59]
	v_lshl_add_u64 v[68:69], v[144:145], 1, s[60:61]
	global_load_dwordx4 v[102:105], v[66:67], off offset:1536
	global_load_dwordx4 v[106:109], v[68:69], off
	v_mov_b32_e32 v0, s50
	ds_read_b32 v0, v0 offset:512
	v_and_b32_e32 v2, 64, v222
	v_add_u32_e32 v2, 64, v2
	s_waitcnt lgkmcnt(0)
	v_mul_f32_e32 v12, 0x3e8293ee, v0
	v_xor_b32_e32 v0, 32, v222
	v_cmp_lt_i32_e32 vcc, v0, v2
	s_waitcnt vmcnt(7)
	v_lshlrev_b32_e32 v2, 16, v6
	v_and_b32_e32 v3, 0xffff0000, v6
	v_pk_mul_f32 v[10:11], v[2:3], s[92:93] op_sel_hi:[1,0]
	v_pk_mul_f32 v[2:3], v[2:3], v[2:3]
	v_cvt_pk_bf16_f32 v6, v10, v11
	v_lshlrev_b32_e32 v10, 16, v7
	v_and_b32_e32 v11, 0xffff0000, v7
	v_pk_mul_f32 v[14:15], v[10:11], s[92:93] op_sel_hi:[1,0]
	v_add_f32_e32 v2, v2, v3
	v_cvt_pk_bf16_f32 v7, v14, v15
	v_lshlrev_b32_e32 v14, 16, v8
	v_and_b32_e32 v15, 0xffff0000, v8
	v_pk_mul_f32 v[16:17], v[14:15], s[92:93] op_sel_hi:[1,0]
	v_cndmask_b32_e32 v0, v222, v0, vcc
	v_cvt_pk_bf16_f32 v8, v16, v17
	v_lshlrev_b32_e32 v16, 16, v9
	v_and_b32_e32 v17, 0xffff0000, v9
	v_pk_mul_f32 v[18:19], v[16:17], s[92:93] op_sel_hi:[1,0]
	v_lshlrev_b32_e32 v190, 2, v0
	v_cvt_pk_bf16_f32 v9, v18, v19
	ds_write_b128 v189, v[6:9] offset:40960
	v_pk_mul_f32 v[8:9], v[10:11], v[10:11]
	v_pk_mul_f32 v[6:7], v[14:15], v[14:15]
	v_pk_mul_f32 v[10:11], v[16:17], v[16:17]
	v_add_f32_e32 v8, v8, v9
	v_add_f32_e32 v2, v2, v8
	v_add_f32_e32 v3, v6, v7
	v_add_f32_e32 v0, v10, v11
	v_add_f32_e32 v2, v3, v2
	v_add_f32_e32 v0, v0, v2
	s_waitcnt vmcnt(6)
	v_mov_b64_e32 v[14:15], v[112:113]
	v_mov_b64_e32 v[16:17], v[114:115]
	v_lshlrev_b32_e32 v18, 16, v14
	v_and_b32_e32 v19, 0xffff0000, v14
	v_pk_mul_f32 v[20:21], v[18:19], s[92:93] op_sel_hi:[1,0]
	s_nop 0
	v_cvt_pk_bf16_f32 v14, v20, v21
	v_lshlrev_b32_e32 v20, 16, v15
	v_and_b32_e32 v21, 0xffff0000, v15
	v_pk_mul_f32 v[22:23], v[20:21], s[92:93] op_sel_hi:[1,0]
	s_nop 0
	v_cvt_pk_bf16_f32 v15, v22, v23
	v_lshlrev_b32_e32 v22, 16, v16
	v_and_b32_e32 v23, 0xffff0000, v16
	v_pk_mul_f32 v[24:25], v[22:23], s[92:93] op_sel_hi:[1,0]
	s_nop 0
	v_cvt_pk_bf16_f32 v16, v24, v25
	v_lshlrev_b32_e32 v24, 16, v17
	v_and_b32_e32 v25, 0xffff0000, v17
	v_pk_mul_f32 v[26:27], v[24:25], s[92:93] op_sel_hi:[1,0]
	s_nop 0
	v_cvt_pk_bf16_f32 v17, v26, v27
	ds_write_b128 v189, v[14:17] offset:41984
	v_pk_mul_f32 v[14:15], v[18:19], v[18:19]
	v_pk_mul_f32 v[16:17], v[20:21], v[20:21]
	v_add_f32_e32 v2, v14, v15
	v_pk_mul_f32 v[18:19], v[22:23], v[22:23]
	v_add_f32_e32 v0, v2, v0
	v_add_f32_e32 v2, v16, v17
	v_pk_mul_f32 v[20:21], v[24:25], v[24:25]
	v_add_f32_e32 v0, v2, v0
	v_add_f32_e32 v2, v18, v19
	v_add_f32_e32 v0, v2, v0
	v_add_f32_e32 v2, v20, v21
	v_add_f32_e32 v2, v2, v0
	v_mov_b32_e32 v0, s28
	ds_bpermute_b32 v3, v190, v2
	v_mov_b32_e32 v18, 0
	v_mov_b32_e32 v0, 0
	s_and_saveexec_b64 s[28:29], s[4:5]
	s_cbranch_execz .LBB0_777
	s_waitcnt lgkmcnt(0)
	v_add_f32_e32 v0, v2, v3
	s_waitcnt vmcnt(5)
	v_mul_f32_e32 v0, v0, v124
	s_mov_b32 s0, 0xf800000
	v_mul_f32_e32 v2, 0x4f800000, v0
	v_cmp_gt_f32_e32 vcc, s0, v0
	s_nop 1
	v_cndmask_b32_e32 v0, v0, v2, vcc
	v_sqrt_f32_e32 v2, v0
	s_nop 0
	v_add_u32_e32 v3, -1, v2
	v_fma_f32 v7, -v3, v2, v0
	v_add_u32_e32 v6, 1, v2
	v_cmp_ge_f32_e64 s[0:1], 0, v7
	s_nop 1
	v_cndmask_b32_e64 v3, v2, v3, s[0:1]
	v_fma_f32 v2, -v6, v2, v0
	v_cmp_lt_f32_e64 s[0:1], 0, v2
	s_nop 1
	v_cndmask_b32_e64 v2, v3, v6, s[0:1]
	v_mov_b32_e32 v3, s50
	ds_read_b32 v3, v3 offset:516
	v_mul_f32_e32 v6, 0x37800000, v2
	v_cndmask_b32_e32 v2, v2, v6, vcc
	v_cmp_class_f32_e32 vcc, v0, v250
	s_nop 1
	v_cndmask_b32_e32 v0, v2, v0, vcc
	s_waitcnt lgkmcnt(0)
	v_fmac_f32_e32 v3, 0x3f8020c5, v0
	v_fmamk_f32 v0, v3, 0xbe8293ee, v12
	v_cvt_pk_bf16_f32 v0, v0, 0
	v_and_b32_e32 v0, 0xffff, v0
; #define LAS __attribute__((address_space(3)))
; __device__ __forceinline__ float bflo(unsigned w) { return __uint_as_float(w << 16); }
; __device__ __forceinline__ float bfhi(unsigned w) { return __uint_as_float(w & 0xFFFF0000u); }
; __device__ __forceinline__ unsigned pkbf(float lo, float hi) { f32x2_t v = {lo, hi}; bf16x2_t b = __builtin_convertvector(v, bf16x2_t); return __builtin_bit_cast(unsigned, b); }
;     ...
;               for (int s = 0; s < 2; ++s) { const u32x4 qv = *(const u32x4*)(U + qrow * INW + C_QD + h * 64 + c * 32 + s * 16 + hi * 8);
;                   const unsigned qw[4] = {qv.x, qv.y, qv.z, qv.w};
;                   { u32x4 qs; qs.x = pkbf(bflo(qw[0]) * c2, bfhi(qw[0]) * c2); qs.y = pkbf(bflo(qw[1]) * c2, bfhi(qw[1]) * c2); qs.z = pkbf(bflo(qw[2]) * c2, bfhi(qw[2]) * c2); qs.w = pkbf(bflo(qw[3]) * c2, bfhi(qw[3]) * c2);
;                     Qs[(c * 2 + s) * 64] = __builtin_bit_cast(bf16x8, qs); }
; #pragma unroll
;                   for (int e = 0; e < 4; ++e) qn2 += bflo(qw[e]) * bflo(qw[e]) + bfhi(qw[e]) * bfhi(qw[e]); }
;               qn2 += __shfl_xor(qn2, 32);
;               const float km2 = __uint_as_float(__hip_atomic_load(kmx + c, __ATOMIC_RELAXED, __HIP_MEMORY_SCOPE_AGENT));
;               mref[c] = (sqrtf(qn2 * km2) * 1.001f + btab[h * 132 + 129]) * c2;
;               { u32x4 qx; qx.x = hi ? 0u : (pkbf(farb - mref[c], 0.f) & 0xffffu); qx.y = 0u; qx.z = 0u; qx.w = 0u; Qs[(4 + c) * 64] = __builtin_bit_cast(bf16x8, qx); } } }
;         f32x16 O[2][2]; float lsum[2] = {0.f, 0.f};
; #pragma unroll
;         for (int c = 0; c < 2; ++c)
; #pragma unroll
;             for (int d = 0; d < 2; ++d)
; #pragma unroll
;                 for (int r = 0; r < 16; ++r) O[c][d][r] = 0.f;
;         const bf16_t* kbase = U + (size_t)b * LT * INW + C_KD + h * 64;
;         const bf16_t* vbase = VT + (size_t)bh * 64 * LTP;
;         const unsigned koff = (unsigned)(krow * INW + kch * 8), voff = (unsigned)(krow * LTP + kch * 8);
;         const float farraw = btab[h * 132 + 128];
;         u32x4 kreg = *(const u32x4*)(kbase + koff), vreg = *(const u32x4*)(vbase + voff);
;         *(LAS u32x4*)(KV + krow * DF_PITCH + kch * 16) = kreg; *(LAS u32x4*)(KV + 2 * DF_KB + krow * DF_PITCH + kch * 16) = vreg;
;         __syncthreads();
.LBB0_777:
	s_or_b64 exec, exec, s[28:29]
	v_mov_b32_e32 v2, v1
	s_waitcnt lgkmcnt(0)
	v_mov_b32_e32 v3, v1
	ds_write_b128 v189, v[0:3] offset:45056
	s_mov_b32 s51, 0
	s_waitcnt vmcnt(4)
	v_mov_b64_e32 v[6:7], v[116:117]
	v_mov_b64_e32 v[8:9], v[118:119]
	v_lshlrev_b32_e32 v2, 16, v6
	v_and_b32_e32 v3, 0xffff0000, v6
	v_pk_mul_f32 v[10:11], v[2:3], s[92:93] op_sel_hi:[1,0]
	v_pk_mul_f32 v[2:3], v[2:3], v[2:3]
	v_cvt_pk_bf16_f32 v6, v10, v11
	v_lshlrev_b32_e32 v10, 16, v7
	v_and_b32_e32 v11, 0xffff0000, v7
	v_pk_mul_f32 v[14:15], v[10:11], s[92:93] op_sel_hi:[1,0]
	v_add_f32_e32 v2, v2, v3
	v_cvt_pk_bf16_f32 v7, v14, v15
	v_lshlrev_b32_e32 v14, 16, v8
	v_and_b32_e32 v15, 0xffff0000, v8
	v_pk_mul_f32 v[16:17], v[14:15], s[92:93] op_sel_hi:[1,0]
	s_nop 0
	v_cvt_pk_bf16_f32 v8, v16, v17
	v_lshlrev_b32_e32 v16, 16, v9
	v_and_b32_e32 v17, 0xffff0000, v9
	v_pk_mul_f32 v[20:21], v[16:17], s[92:93] op_sel_hi:[1,0]
	s_nop 0
	v_cvt_pk_bf16_f32 v9, v20, v21
	ds_write_b128 v189, v[6:9] offset:43008
	v_pk_mul_f32 v[8:9], v[10:11], v[10:11]
	v_pk_mul_f32 v[6:7], v[14:15], v[14:15]
	v_pk_mul_f32 v[10:11], v[16:17], v[16:17]
	v_add_f32_e32 v8, v8, v9
	v_add_f32_e32 v2, v2, v8
	v_add_f32_e32 v3, v6, v7
	v_add_f32_e32 v2, v3, v2
	v_add_f32_e32 v0, v10, v11
	v_add_f32_e32 v0, v0, v2
	s_waitcnt vmcnt(3)
	v_mov_b64_e32 v[14:15], v[120:121]
	v_mov_b64_e32 v[16:17], v[122:123]
	v_lshlrev_b32_e32 v4, 16, v14
	v_and_b32_e32 v5, 0xffff0000, v14
	v_pk_mul_f32 v[20:21], v[4:5], s[92:93] op_sel_hi:[1,0]
	v_pk_mul_f32 v[4:5], v[4:5], v[4:5]
	v_cvt_pk_bf16_f32 v14, v20, v21
	v_lshlrev_b32_e32 v20, 16, v15
	v_and_b32_e32 v21, 0xffff0000, v15
	v_pk_mul_f32 v[22:23], v[20:21], s[92:93] op_sel_hi:[1,0]
	v_add_f32_e32 v2, v4, v5
	v_cvt_pk_bf16_f32 v15, v22, v23
	v_lshlrev_b32_e32 v22, 16, v16
	v_and_b32_e32 v23, 0xffff0000, v16
	v_pk_mul_f32 v[24:25], v[22:23], s[92:93] op_sel_hi:[1,0]
	v_add_f32_e32 v0, v2, v0
	v_cvt_pk_bf16_f32 v16, v24, v25
	v_lshlrev_b32_e32 v24, 16, v17
	v_and_b32_e32 v25, 0xffff0000, v17
	v_pk_mul_f32 v[26:27], v[24:25], s[92:93] op_sel_hi:[1,0]
	s_nop 0
	v_cvt_pk_bf16_f32 v17, v26, v27
	ds_write_b128 v189, v[14:17] offset:44032
	v_pk_mul_f32 v[14:15], v[20:21], v[20:21]
	v_pk_mul_f32 v[16:17], v[22:23], v[22:23]
	v_add_f32_e32 v2, v14, v15
	v_pk_mul_f32 v[20:21], v[24:25], v[24:25]
	v_add_f32_e32 v0, v2, v0
	v_add_f32_e32 v2, v16, v17
	v_add_f32_e32 v0, v2, v0
	v_add_f32_e32 v2, v20, v21
	v_add_f32_e32 v0, v2, v0
	ds_bpermute_b32 v2, v190, v0
	s_and_saveexec_b64 s[24:25], s[4:5]
	s_cbranch_execz .LBB0_779
	s_waitcnt lgkmcnt(0)
	v_add_f32_e32 v0, v0, v2
	s_waitcnt vmcnt(2)
	v_mul_f32_e32 v0, v0, v126
	s_mov_b32 s0, 0xf800000
	v_mul_f32_e32 v2, 0x4f800000, v0
	v_cmp_gt_f32_e32 vcc, s0, v0
	s_nop 1
	v_cndmask_b32_e32 v0, v0, v2, vcc
	v_sqrt_f32_e32 v2, v0
	s_nop 0
	v_add_u32_e32 v3, -1, v2
	v_fma_f32 v5, -v3, v2, v0
	v_add_u32_e32 v4, 1, v2
	v_cmp_ge_f32_e64 s[0:1], 0, v5
	s_nop 1
	v_cndmask_b32_e64 v3, v2, v3, s[0:1]
	v_fma_f32 v2, -v4, v2, v0
	v_cmp_lt_f32_e64 s[0:1], 0, v2
	s_nop 1
	v_cndmask_b32_e64 v2, v3, v4, s[0:1]
	v_mov_b32_e32 v3, s50
	ds_read_b32 v3, v3 offset:516
	v_mul_f32_e32 v4, 0x37800000, v2
	v_cndmask_b32_e32 v2, v2, v4, vcc
	v_cmp_class_f32_e32 vcc, v0, v250
	s_nop 1
	v_cndmask_b32_e32 v0, v2, v0, vcc
	s_waitcnt lgkmcnt(0)
	v_fmac_f32_e32 v3, 0x3f8020c5, v0
	v_fmac_f32_e32 v12, 0xbe8293ee, v3
	v_cvt_pk_bf16_f32 v0, v12, 0
	v_and_b32_e32 v18, 0xffff, v0
.LBB0_779:
	s_or_b64 exec, exec, s[24:25]
	s_sub_i32 s37, 0, s35
	s_lshl_b32 s0, s36, 6
	s_cmpk_lt_i32 s30, 0x200
	s_cselect_b64 s[24:25], -1, 0
	s_lshl_b32 s52, s31, 2
	s_or_b64 s[28:29], s[24:25], s[18:19]
	s_mul_i32 s30, s22, 0x1600
	s_mul_hi_i32 s1, s22, 0x1600
	s_add_u32 s30, s8, s30
	s_addc_u32 s1, s9, s1
	s_lshl_b32 s40, s0, 1
	s_add_u32 s30, s30, s40
	s_mul_i32 s0, s34, 0x41000
	s_addc_u32 s31, s1, 0
	s_ashr_i32 s1, s0, 31
	s_lshl_b64 s[0:1], s[0:1], 1
	s_add_u32 s34, s42, s0
	s_addc_u32 s35, s43, s1
	s_waitcnt vmcnt(2) lgkmcnt(0)
	v_lshl_add_u64 v[2:3], v[142:143], 1, s[30:31]
	v_lshl_add_u64 v[4:5], v[144:145], 1, s[34:35]
	v_mov_b32_e32 v19, v1
	v_mov_b32_e32 v20, v1
	v_mov_b32_e32 v21, v1
	v_mov_b32_e32 v22, s50
	ds_write_b128 v189, v[18:21] offset:46080
	ds_read_b32 v150, v22 offset:512
	v_mov_b32_e32 v16, v1
	v_mov_b32_e32 v17, v1
	v_mov_b32_e32 v2, v1
	v_mov_b32_e32 v3, v1
	v_mov_b32_e32 v4, v1
	v_mov_b32_e32 v5, v1
	v_mov_b32_e32 v6, v1
	v_mov_b32_e32 v7, v1
	v_mov_b32_e32 v8, v1
	v_mov_b32_e32 v9, v1
	v_mov_b32_e32 v10, v1
	v_mov_b32_e32 v11, v1
	v_mov_b32_e32 v12, v1
	v_mov_b32_e32 v13, v1
	v_mov_b32_e32 v14, v1
	v_mov_b32_e32 v15, v1
	v_mov_b64_e32 v[48:49], v[16:17]
	v_mov_b64_e32 v[32:33], v[16:17]
	v_mov_b64_e32 v[64:65], v[16:17]
	s_lshl_b32 s55, s37, 2
	v_mov_b32_e32 v147, v148
	v_mov_b32_e32 v191, 0
	v_add_u32_e32 v0, 0x2c000, v142
	v_mov_b32_e32 v192, 0
	v_mov_b64_e32 v[46:47], v[14:15]
	v_mov_b64_e32 v[44:45], v[12:13]
	v_mov_b64_e32 v[42:43], v[10:11]
	v_mov_b64_e32 v[40:41], v[8:9]
	v_mov_b64_e32 v[38:39], v[6:7]
	v_mov_b64_e32 v[36:37], v[4:5]
	v_mov_b64_e32 v[34:35], v[2:3]
	v_mov_b64_e32 v[30:31], v[14:15]
	v_mov_b64_e32 v[28:29], v[12:13]
	v_mov_b64_e32 v[26:27], v[10:11]
	v_mov_b64_e32 v[24:25], v[8:9]
	v_mov_b64_e32 v[22:23], v[6:7]
	v_mov_b64_e32 v[20:21], v[4:5]
	v_mov_b64_e32 v[18:19], v[2:3]
	v_mov_b64_e32 v[62:63], v[14:15]
	v_mov_b64_e32 v[60:61], v[12:13]
	v_mov_b64_e32 v[58:59], v[10:11]
	v_mov_b64_e32 v[56:57], v[8:9]
	v_mov_b64_e32 v[54:55], v[6:7]
	v_mov_b64_e32 v[52:53], v[4:5]
	v_mov_b64_e32 v[50:51], v[2:3]
	s_waitcnt lgkmcnt(0)
	v_mov_b32_e32 v151, v150
	s_add_i32 s53, s49, 31
	s_sub_i32 s54, s49, 63
	s_addk_i32 s55, 0x41
	s_mov_b32 s56, 0
	s_waitcnt vmcnt(1)
	ds_write_b128 v185, v[102:105] offset:4096
	s_waitcnt vmcnt(0)
	ds_write_b128 v185, v[106:109] offset:22528
	s_waitcnt lgkmcnt(0)
	s_barrier
	s_branch .LBB0_781
